# prologue weight-conversion tiles: the 8 masked loads of each 64x64 tile issued together with one wait (on top of v15)
# speedup vs baseline: 1.1120x; 1.0048x over previous
.Lwc_b_tail:
	v_ashrrev_i32_e32 v9, 3, v1
	v_lshlrev_b32_e32 v1, 3, v1
	v_and_b32_e32 v6, 56, v1
	v_mul_u32_u24_e32 v1, 0x104, v6
	v_lshlrev_b32_e32 v2, 2, v9
	v_add3_u32 v1, 0, v1, v2
	s_waitcnt lgkmcnt(0)
	s_barrier
	ds_read2_b32 v[2:3], v1 offset1:65
	s_mul_hi_i32 s49, s70, 0x580000
	s_mul_i32 s70, s70, 0x580000
	s_add_u32 s50, s37, s70
	s_addc_u32 s51, s56, s49
	s_waitcnt lgkmcnt(0)
	v_bfe_u32 v4, v2, 16, 1
	v_add3_u32 v2, v2, v4, s63
	ds_read2_b32 v[4:5], v1 offset0:130 offset1:195
	v_bfe_u32 v10, v3, 16, 1
	v_add_u32_e32 v1, 0x400, v1
	v_add3_u32 v3, v3, v10, s63
	ds_read2_b32 v[10:11], v1 offset0:4 offset1:69
	v_lshrrev_b32_e32 v2, 16, v2
	v_and_or_b32 v2, v3, s64, v2
	s_waitcnt lgkmcnt(1)
	v_bfe_u32 v3, v4, 16, 1
	v_add3_u32 v3, v4, v3, s63
	v_bfe_u32 v4, v5, 16, 1
	v_lshrrev_b32_e32 v3, 16, v3
	v_add3_u32 v4, v5, v4, s63
	ds_read2_b32 v[12:13], v1 offset0:134 offset1:199
	v_and_or_b32 v3, v4, s64, v3
	s_waitcnt lgkmcnt(1)
	v_bfe_u32 v4, v10, 16, 1
	v_add3_u32 v4, v10, v4, s63
	v_lshrrev_b32_e32 v1, 16, v4
	v_bfe_u32 v4, v11, 16, 1
	v_add3_u32 v4, v11, v4, s63
	v_add_u32_e32 v10, s44, v9
	v_and_or_b32 v4, v4, s64, v1
	s_waitcnt lgkmcnt(0)
	v_bfe_u32 v1, v12, 16, 1
	v_ashrrev_i32_e32 v11, 31, v10
	v_add3_u32 v1, v12, v1, s63
	v_bfe_u32 v5, v13, 16, 1
	v_lshlrev_b64 v[10:11], 11, v[10:11]
	v_lshrrev_b32_e32 v1, 16, v1
	v_add3_u32 v5, v13, v5, s63
	v_lshl_add_u64 v[10:11], s[50:51], 0, v[10:11]
	s_ashr_i32 s49, s48, 31
	v_and_or_b32 v5, v5, s64, v1
	v_lshl_add_u64 v[10:11], s[48:49], 1, v[10:11]

.LBB0_13:
	s_cmpk_gt_i32 s69, 0xaff
	s_mov_b64 s[48:49], -1
	s_cbranch_scc0 .LBB0_47
	s_add_i32 s44, s69, 0xfffff500
	s_lshr_b32 s44, s44, 8
	s_lshl_b64 s[48:49], s[44:45], 22
	s_add_u32 s48, s24, s48
	v_mov_b32_e32 v1, v0
	s_addc_u32 s49, s25, s49
	s_and_b32 s51, s57, 0x3c0
	s_and_b32 s50, s59, 0x3c0
	v_and_b32_e32 v9, 63, v1
	v_or_b32_e32 v2, s51, v9
	v_lshlrev_b32_e32 v6, 2, v2
	v_lshl_add_u64 v[2:3], s[48:49], 0, v[6:7]
	v_ashrrev_i32_e32 v6, 6, v1
	s_barrier
	v_lshl_add_u32 v4, v9, 2, 0
	v_mul_lo_u32 v9, v6, s62
	v_add_u32_e32 v9, v4, v9
	v_mov_b32_e32 v14, 0
	v_mov_b32_e32 v15, 0
	v_mov_b32_e32 v16, 0
	v_mov_b32_e32 v17, 0
	v_mov_b32_e32 v18, 0
	v_mov_b32_e32 v19, 0
	v_mov_b32_e32 v20, 0
	v_mov_b32_e32 v21, 0
	s_and_b64 vcc, exec, s[0:1]
	s_cbranch_vccnz .Lwc_a_store
	s_mov_b64 s[74:75], exec
	v_add_u32_e32 v4, s50, v6
	v_cmp_gt_i32_e32 vcc, s61, v4
	s_and_b64 exec, s[74:75], vcc
	v_ashrrev_i32_e32 v5, 31, v4
	v_lshlrev_b64 v[4:5], 12, v[4:5]
	v_lshl_add_u64 v[4:5], v[2:3], 0, v[4:5]
	global_load_dword v14, v[4:5], off
	v_add3_u32 v4, v6, s50, 8
	v_cmp_gt_i32_e32 vcc, s61, v4
	s_and_b64 exec, s[74:75], vcc
	v_ashrrev_i32_e32 v5, 31, v4
	v_lshlrev_b64 v[4:5], 12, v[4:5]
	v_lshl_add_u64 v[4:5], v[2:3], 0, v[4:5]
	global_load_dword v15, v[4:5], off
	v_add3_u32 v4, v6, s50, 16
	v_cmp_gt_i32_e32 vcc, s61, v4
	s_and_b64 exec, s[74:75], vcc
	v_ashrrev_i32_e32 v5, 31, v4
	v_lshlrev_b64 v[4:5], 12, v[4:5]
	v_lshl_add_u64 v[4:5], v[2:3], 0, v[4:5]
	global_load_dword v16, v[4:5], off
	v_add3_u32 v4, v6, s50, 24
	v_cmp_gt_i32_e32 vcc, s61, v4
	s_and_b64 exec, s[74:75], vcc
	v_ashrrev_i32_e32 v5, 31, v4
	v_lshlrev_b64 v[4:5], 12, v[4:5]
	v_lshl_add_u64 v[4:5], v[2:3], 0, v[4:5]
	global_load_dword v17, v[4:5], off
	v_add3_u32 v4, v6, s50, 32
	v_cmp_gt_i32_e32 vcc, s61, v4
	s_and_b64 exec, s[74:75], vcc
	v_ashrrev_i32_e32 v5, 31, v4
	v_lshlrev_b64 v[4:5], 12, v[4:5]
	v_lshl_add_u64 v[4:5], v[2:3], 0, v[4:5]
	global_load_dword v18, v[4:5], off
	v_add3_u32 v4, v6, s50, 40
	v_cmp_gt_i32_e32 vcc, s61, v4
	s_and_b64 exec, s[74:75], vcc
	v_ashrrev_i32_e32 v5, 31, v4
	v_lshlrev_b64 v[4:5], 12, v[4:5]
	v_lshl_add_u64 v[4:5], v[2:3], 0, v[4:5]
	global_load_dword v19, v[4:5], off
	v_add3_u32 v4, v6, s50, 48
	v_cmp_gt_i32_e32 vcc, s61, v4
	s_and_b64 exec, s[74:75], vcc
	v_ashrrev_i32_e32 v5, 31, v4
	v_lshlrev_b64 v[4:5], 12, v[4:5]
	v_lshl_add_u64 v[4:5], v[2:3], 0, v[4:5]
	global_load_dword v20, v[4:5], off
	v_add3_u32 v4, v6, s50, 56
	v_cmp_gt_i32_e32 vcc, s61, v4
	s_and_b64 exec, s[74:75], vcc
	v_ashrrev_i32_e32 v5, 31, v4
	v_lshlrev_b64 v[4:5], 12, v[4:5]
	v_lshl_add_u64 v[4:5], v[2:3], 0, v[4:5]
	global_load_dword v21, v[4:5], off
	s_mov_b64 exec, s[74:75]
.Lwc_a_store:
	s_waitcnt vmcnt(0)
	ds_write_b32 v9, v14
	ds_write_b32 v9, v15 offset:2080
	ds_write_b32 v9, v16 offset:4160
	ds_write_b32 v9, v17 offset:6240
	ds_write_b32 v9, v18 offset:8320
	ds_write_b32 v9, v19 offset:10400
	ds_write_b32 v9, v20 offset:12480
	ds_write_b32 v9, v21 offset:14560
	v_ashrrev_i32_e32 v9, 3, v1
	v_lshlrev_b32_e32 v1, 3, v1
	v_and_b32_e32 v6, 56, v1
	v_mul_u32_u24_e32 v1, 0x104, v6
	v_lshlrev_b32_e32 v2, 2, v9
	v_add3_u32 v1, 0, v1, v2
	s_waitcnt lgkmcnt(0)
	s_barrier
	ds_read2_b32 v[2:3], v1 offset1:65
	s_lshl_b64 s[48:49], s[44:45], 20
	s_lshl_b64 s[48:49], s[48:49], 1
	s_add_u32 s48, s3, s48
	s_addc_u32 s49, s33, s49
	s_waitcnt lgkmcnt(0)
	v_bfe_u32 v4, v2, 16, 1
	v_add3_u32 v2, v2, v4, s63
	ds_read2_b32 v[4:5], v1 offset0:130 offset1:195
	v_bfe_u32 v10, v3, 16, 1
	v_add_u32_e32 v1, 0x400, v1
	v_add3_u32 v3, v3, v10, s63
	ds_read2_b32 v[10:11], v1 offset0:4 offset1:69
	v_lshrrev_b32_e32 v2, 16, v2
	v_and_or_b32 v2, v3, s64, v2
	s_waitcnt lgkmcnt(1)
	v_bfe_u32 v3, v4, 16, 1
	v_add3_u32 v3, v4, v3, s63
	v_bfe_u32 v4, v5, 16, 1
	v_lshrrev_b32_e32 v3, 16, v3
	v_add3_u32 v4, v5, v4, s63
	ds_read2_b32 v[12:13], v1 offset0:134 offset1:199
	v_and_or_b32 v3, v4, s64, v3
	s_waitcnt lgkmcnt(1)
	v_bfe_u32 v4, v10, 16, 1
	v_add3_u32 v4, v10, v4, s63
	v_lshrrev_b32_e32 v1, 16, v4
	v_bfe_u32 v4, v11, 16, 1
	v_add3_u32 v4, v11, v4, s63
	v_add_u32_e32 v10, s51, v9
	v_and_or_b32 v4, v4, s64, v1
	s_waitcnt lgkmcnt(0)
	v_bfe_u32 v1, v12, 16, 1
	v_ashrrev_i32_e32 v11, 31, v10
	v_add3_u32 v1, v12, v1, s63
	v_bfe_u32 v5, v13, 16, 1
	v_lshlrev_b64 v[10:11], 11, v[10:11]
	v_lshrrev_b32_e32 v1, 16, v1
	v_add3_u32 v5, v13, v5, s63
	v_lshl_add_u64 v[10:11], s[48:49], 0, v[10:11]
	s_lshl_b32 s44, s50, 1
	v_and_or_b32 v5, v5, s64, v1
	v_lshl_add_u64 v[10:11], v[10:11], 0, s[44:45]
	s_mov_b64 s[48:49], 0

.LBB0_66:
	s_or_b64 exec, exec, s[48:49]
	s_lshl_b32 s48, s55, 4
	s_sub_i32 s48, s54, s48
	s_mul_i32 s50, s70, 0xaec000
	s_mul_hi_i32 s49, s70, 0xaec000
	s_add_u32 s50, s42, s50
	s_sext_i32_i16 s48, s48
	s_addc_u32 s51, s43, s49
	v_cmp_lt_i32_e32 vcc, -1, v6
	s_lshl_b32 s48, s48, 6
	v_lshl_add_u64 v[2:3], v[6:7], 2, s[50:51]
	v_ashrrev_i32_e32 v4, 6, v1
	s_and_b64 s[50:51], vcc, s[46:47]
	v_lshl_add_u32 v5, v5, 2, 0
	v_mul_lo_u32 v10, v4, s62
	v_add_u32_e32 v5, v5, v10
	v_mov_b32_e32 v14, 0
	v_mov_b32_e32 v15, 0
	v_mov_b32_e32 v16, 0
	v_mov_b32_e32 v17, 0
	v_mov_b32_e32 v18, 0
	v_mov_b32_e32 v19, 0
	v_mov_b32_e32 v20, 0
	v_mov_b32_e32 v21, 0
	s_mov_b64 s[74:75], exec
	v_add_u32_e32 v9, s48, v4
	v_cmp_gt_i32_e32 vcc, s61, v9
	s_and_b64 vcc, vcc, s[50:51]
	s_and_b64 exec, s[74:75], vcc
	v_mad_i64_i32 v[10:11], s[72:73], v9, s68, v[2:3]
	global_load_dword v14, v[10:11], off
	v_add3_u32 v9, v4, s48, 8
	v_cmp_gt_i32_e32 vcc, s61, v9
	s_and_b64 vcc, vcc, s[50:51]
	s_and_b64 exec, s[74:75], vcc
	v_mad_i64_i32 v[10:11], s[72:73], v9, s68, v[2:3]
	global_load_dword v15, v[10:11], off
	v_add3_u32 v9, v4, s48, 16
	v_cmp_gt_i32_e32 vcc, s61, v9
	s_and_b64 vcc, vcc, s[50:51]
	s_and_b64 exec, s[74:75], vcc
	v_mad_i64_i32 v[10:11], s[72:73], v9, s68, v[2:3]
	global_load_dword v16, v[10:11], off
	v_add3_u32 v9, v4, s48, 24
	v_cmp_gt_i32_e32 vcc, s61, v9
	s_and_b64 vcc, vcc, s[50:51]
	s_and_b64 exec, s[74:75], vcc
	v_mad_i64_i32 v[10:11], s[72:73], v9, s68, v[2:3]
	global_load_dword v17, v[10:11], off
	v_add3_u32 v9, v4, s48, 32
	v_cmp_gt_i32_e32 vcc, s61, v9
	s_and_b64 vcc, vcc, s[50:51]
	s_and_b64 exec, s[74:75], vcc
	v_mad_i64_i32 v[10:11], s[72:73], v9, s68, v[2:3]
	global_load_dword v18, v[10:11], off
	v_add3_u32 v9, v4, s48, 40
	v_cmp_gt_i32_e32 vcc, s61, v9
	s_and_b64 vcc, vcc, s[50:51]
	s_and_b64 exec, s[74:75], vcc
	v_mad_i64_i32 v[10:11], s[72:73], v9, s68, v[2:3]
	global_load_dword v19, v[10:11], off
	v_add3_u32 v9, v4, s48, 48
	v_cmp_gt_i32_e32 vcc, s61, v9
	s_and_b64 vcc, vcc, s[50:51]
	s_and_b64 exec, s[74:75], vcc
	v_mad_i64_i32 v[10:11], s[72:73], v9, s68, v[2:3]
	global_load_dword v20, v[10:11], off
	v_add3_u32 v9, v4, s48, 56
	v_cmp_gt_i32_e32 vcc, s61, v9
	s_and_b64 vcc, vcc, s[50:51]
	s_and_b64 exec, s[74:75], vcc
	v_mad_i64_i32 v[10:11], s[72:73], v9, s68, v[2:3]
	global_load_dword v21, v[10:11], off
	s_mov_b64 exec, s[74:75]
	s_waitcnt vmcnt(0)
	ds_write_b32 v5, v14
	ds_write_b32 v5, v15 offset:2080
	ds_write_b32 v5, v16 offset:4160
	ds_write_b32 v5, v17 offset:6240
	ds_write_b32 v5, v18 offset:8320
	ds_write_b32 v5, v19 offset:10400
	ds_write_b32 v5, v20 offset:12480
	ds_write_b32 v5, v21 offset:14560
	s_branch .Lwc_b_tail
